# DeltaNet conv passes: 16-lane sums by DPP row operations instead of serialized ds_bpermute round trips
# speedup vs baseline: 1.0005x; 1.0005x over previous
.LBB0_327:
	s_waitcnt vmcnt(11)
	v_mov_b64_e32 v[78:79], v[24:25]
	v_lshlrev_b32_e32 v62, 16, v50
	v_and_b32_e32 v63, 0xffff0000, v50
	v_mov_b64_e32 v[76:77], v[22:23]
	v_lshlrev_b32_e32 v22, 16, v58
	v_and_b32_e32 v23, 0xffff0000, v58
	s_waitcnt vmcnt(5)
	v_pk_mul_f32 v[24:25], v[14:15], v[62:63]
	v_lshlrev_b32_e32 v72, 16, v76
	v_pk_fma_f32 v[22:23], v[6:7], v[22:23], v[24:25]
	v_and_b32_e32 v73, 0xffff0000, v76
	s_waitcnt vmcnt(3)
	v_pk_fma_f32 v[22:23], v[26:27], v[72:73], v[22:23]
	v_lshlrev_b32_e32 v68, 16, v46
	v_and_b32_e32 v69, 0xffff0000, v46
	s_waitcnt vmcnt(1) lgkmcnt(1)
	v_pk_fma_f32 v[36:37], v[38:39], v[68:69], v[22:23]
	v_lshlrev_b32_e32 v74, 16, v77
	v_mul_f32_e32 v0, 0xbfb8aa3b, v36
	v_exp_f32_e32 v0, v0
	v_mul_f32_e32 v22, 0xbfb8aa3b, v37
	v_exp_f32_e32 v23, v22
	v_add_co_u32_e32 v22, vcc, 0xfffe7000, v66
	v_add_f32_e32 v0, 1.0, v0
	v_rcp_f32_e32 v64, v0
	v_add_f32_e32 v0, 1.0, v23
	v_addc_co_u32_e32 v23, vcc, -1, v67, vcc
	global_load_dwordx4 v[22:25], v[22:23], off offset:-3584
	v_rcp_f32_e32 v65, v0
	v_and_b32_e32 v75, 0xffff0000, v77
	v_lshlrev_b32_e32 v58, 16, v47
	v_lshlrev_b32_e32 v80, 16, v52
	v_pk_mul_f32 v[82:83], v[36:37], v[64:65]
	v_lshlrev_b32_e32 v64, 16, v51
	v_and_b32_e32 v65, 0xffff0000, v51
	v_lshlrev_b32_e32 v36, 16, v59
	v_and_b32_e32 v37, 0xffff0000, v59
	v_pk_mul_f32 v[50:51], v[16:17], v[64:65]
	v_and_b32_e32 v59, 0xffff0000, v47
	v_pk_fma_f32 v[36:37], v[8:9], v[36:37], v[50:51]
	v_and_b32_e32 v81, 0xffff0000, v52
	v_pk_fma_f32 v[36:37], v[28:29], v[74:75], v[36:37]
	v_lshlrev_b32_e32 v70, 16, v60
	v_pk_fma_f32 v[36:37], v[40:41], v[58:59], v[36:37]
	v_and_b32_e32 v71, 0xffff0000, v60
	v_mul_f32_e32 v0, 0xbfb8aa3b, v36
	v_exp_f32_e32 v0, v0
	v_mul_f32_e32 v35, 0xbfb8aa3b, v37
	v_exp_f32_e32 v35, v35
	v_pk_mul_f32 v[76:77], v[18:19], v[80:81]
	v_add_f32_e32 v0, 1.0, v0
	v_rcp_f32_e32 v50, v0
	v_add_f32_e32 v0, 1.0, v35
	v_pk_fma_f32 v[70:71], v[10:11], v[70:71], v[76:77]
	v_lshlrev_b32_e32 v76, 16, v78
	v_and_b32_e32 v77, 0xffff0000, v78
	v_rcp_f32_e32 v51, v0
	v_pk_fma_f32 v[84:85], v[30:31], v[76:77], v[70:71]
	v_lshlrev_b32_e32 v70, 16, v48
	v_and_b32_e32 v71, 0xffff0000, v48
	s_waitcnt vmcnt(1)
	v_pk_fma_f32 v[84:85], v[42:43], v[70:71], v[84:85]
	v_lshlrev_b32_e32 v88, 16, v53
	v_mul_f32_e32 v0, 0xbfb8aa3b, v84
	v_exp_f32_e32 v0, v0
	v_mul_f32_e32 v35, 0xbfb8aa3b, v85
	v_and_b32_e32 v89, 0xffff0000, v53
	v_exp_f32_e32 v35, v35
	v_pk_mul_f32 v[86:87], v[36:37], v[50:51]
	v_lshlrev_b32_e32 v50, 16, v61
	v_and_b32_e32 v51, 0xffff0000, v61
	v_pk_mul_f32 v[52:53], v[20:21], v[88:89]
	v_lshlrev_b32_e32 v78, 16, v79
	v_pk_fma_f32 v[50:51], v[12:13], v[50:51], v[52:53]
	v_and_b32_e32 v79, 0xffff0000, v79
	v_pk_fma_f32 v[50:51], v[32:33], v[78:79], v[50:51]
	v_lshlrev_b32_e32 v60, 16, v49
	v_and_b32_e32 v61, 0xffff0000, v49
	v_add_f32_e32 v0, 1.0, v0
	v_pk_fma_f32 v[48:49], v[44:45], v[60:61], v[50:51]
	v_rcp_f32_e32 v36, v0
	v_add_f32_e32 v0, 1.0, v35
	v_mul_f32_e32 v35, 0xbfb8aa3b, v48
	v_exp_f32_e32 v35, v35
	v_mul_f32_e32 v37, 0xbfb8aa3b, v49
	v_exp_f32_e32 v51, v37
	v_rcp_f32_e32 v37, v0
	v_add_f32_e32 v0, 1.0, v35
	v_rcp_f32_e32 v50, v0
	v_add_f32_e32 v0, 1.0, v51
	v_pk_mul_f32 v[46:47], v[82:83], v[82:83]
	v_rcp_f32_e32 v51, v0
	v_pk_mul_f32 v[52:53], v[86:87], v[86:87]
	v_add_f32_e32 v0, v46, v47
	v_pk_mul_f32 v[84:85], v[84:85], v[36:37]
	v_add_f32_e32 v0, v52, v0
	v_pk_mul_f32 v[36:37], v[84:85], v[84:85]
	v_add_f32_e32 v0, v53, v0
	v_pk_mul_f32 v[90:91], v[48:49], v[50:51]
	v_add_f32_e32 v0, v36, v0
	v_pk_mul_f32 v[48:49], v[90:91], v[90:91]
	v_add_f32_e32 v0, v37, v0
	v_add_f32_e32 v0, v48, v0
	v_add_f32_e32 v0, v49, v0
	s_nop 1
	v_mov_b32_dpp v35, v0 quad_perm:[1,0,3,2] row_mask:0xf bank_mask:0xf
	v_mov_b64_e32 v[50:51], v[54:55]
	v_mov_b64_e32 v[52:53], v[56:57]
	v_cvt_pk_bf16_f32 v46, v82, v83
	v_cvt_pk_bf16_f32 v47, v86, v87
	s_waitcnt lgkmcnt(0)
	v_add_f32_e32 v0, v0, v35
	s_nop 1
	v_mov_b32_dpp v35, v0 quad_perm:[2,3,0,1] row_mask:0xf bank_mask:0xf
	v_cvt_pk_bf16_f32 v48, v84, v85
	v_cvt_pk_bf16_f32 v49, v90, v91
	v_add_u32_e32 v94, 0, v93
	s_waitcnt lgkmcnt(0)
	v_add_f32_e32 v0, v0, v35
	s_nop 1
	v_mov_b32_dpp v35, v0 row_half_mirror row_mask:0xf bank_mask:0xf
	s_waitcnt lgkmcnt(0)
	v_add_f32_e32 v35, v0, v35
	s_nop 1
	v_mov_b32_dpp v36, v35 row_mirror row_mask:0xf bank_mask:0xf
	v_xor_b32_e32 v0, s14, v187
	v_lshlrev_b32_e32 v0, 4, v0
	v_add3_u32 v0, 0, v0, v92
	ds_write_b128 v0, v[46:49]
	s_and_saveexec_b64 s[12:13], s[10:11]
	s_cbranch_execz .LBB0_329
	s_waitcnt lgkmcnt(1)
	v_add_f32_e32 v0, v35, v36
	v_add_u32_e32 v35, 0x20200, v94
	ds_write_b32 v35, v0

.LBB0_332:
	v_pk_mul_f32 v[36:37], v[14:15], v[72:73]
	v_lshlrev_b32_e32 v86, 16, v2
	v_pk_fma_f32 v[36:37], v[6:7], v[62:63], v[36:37]
	v_and_b32_e32 v87, 0xffff0000, v2
	v_pk_fma_f32 v[36:37], v[26:27], v[68:69], v[36:37]
	v_lshlrev_b32_e32 v84, 16, v3
	v_pk_fma_f32 v[36:37], v[38:39], v[86:87], v[36:37]
	v_and_b32_e32 v85, 0xffff0000, v3
	v_mul_f32_e32 v0, 0xbfb8aa3b, v36
	v_exp_f32_e32 v0, v0
	v_mul_f32_e32 v35, 0xbfb8aa3b, v37
	v_exp_f32_e32 v35, v35
	v_lshlrev_b32_e32 v82, 16, v4
	v_add_f32_e32 v0, 1.0, v0
	v_rcp_f32_e32 v54, v0
	v_add_f32_e32 v0, 1.0, v35
	v_rcp_f32_e32 v55, v0
	v_and_b32_e32 v83, 0xffff0000, v4
	v_pk_mul_f32 v[54:55], v[36:37], v[54:55]
	v_pk_mul_f32 v[36:37], v[16:17], v[74:75]
	v_pk_mul_f32 v[56:57], v[54:55], v[54:55]
	v_pk_fma_f32 v[36:37], v[8:9], v[64:65], v[36:37]
	v_pk_mul_f32 v[64:65], v[18:19], v[76:77]
	v_pk_fma_f32 v[36:37], v[28:29], v[58:59], v[36:37]
	v_pk_fma_f32 v[64:65], v[10:11], v[80:81], v[64:65]
	v_pk_fma_f32 v[36:37], v[40:41], v[84:85], v[36:37]
	v_pk_fma_f32 v[64:65], v[30:31], v[70:71], v[64:65]
	v_mul_f32_e32 v0, 0xbfb8aa3b, v36
	v_exp_f32_e32 v0, v0
	v_mul_f32_e32 v35, 0xbfb8aa3b, v37
	v_exp_f32_e32 v35, v35
	v_pk_fma_f32 v[64:65], v[42:43], v[82:83], v[64:65]
	v_add_f32_e32 v0, 1.0, v0
	v_rcp_f32_e32 v62, v0
	v_add_f32_e32 v0, 1.0, v35
	v_rcp_f32_e32 v63, v0
	v_mul_f32_e32 v0, 0xbfb8aa3b, v64
	v_exp_f32_e32 v0, v0
	v_mul_f32_e32 v35, 0xbfb8aa3b, v65
	v_exp_f32_e32 v35, v35
	v_pk_mul_f32 v[80:81], v[20:21], v[78:79]
	v_add_f32_e32 v0, 1.0, v0
	v_pk_fma_f32 v[80:81], v[12:13], v[88:89], v[80:81]
	v_pk_mul_f32 v[62:63], v[36:37], v[62:63]
	v_pk_fma_f32 v[88:89], v[32:33], v[60:61], v[80:81]
	v_lshlrev_b32_e32 v80, 16, v5
	v_and_b32_e32 v81, 0xffff0000, v5
	v_pk_fma_f32 v[88:89], v[44:45], v[80:81], v[88:89]
	v_rcp_f32_e32 v36, v0
	v_add_f32_e32 v0, 1.0, v35
	v_mul_f32_e32 v35, 0xbfb8aa3b, v88
	v_exp_f32_e32 v35, v35
	v_mul_f32_e32 v37, 0xbfb8aa3b, v89
	v_exp_f32_e32 v91, v37
	v_rcp_f32_e32 v37, v0
	v_add_f32_e32 v0, 1.0, v35
	v_rcp_f32_e32 v90, v0
	v_add_f32_e32 v0, 1.0, v91
	v_rcp_f32_e32 v91, v0
	v_pk_mul_f32 v[96:97], v[62:63], v[62:63]
	v_add_f32_e32 v0, v56, v57
	v_pk_mul_f32 v[64:65], v[64:65], v[36:37]
	v_add_f32_e32 v0, v96, v0
	v_pk_mul_f32 v[36:37], v[64:65], v[64:65]
	v_add_f32_e32 v0, v97, v0
	v_pk_mul_f32 v[88:89], v[88:89], v[90:91]
	v_add_f32_e32 v0, v36, v0
	v_pk_mul_f32 v[90:91], v[88:89], v[88:89]
	v_add_f32_e32 v0, v37, v0
	v_add_f32_e32 v0, v90, v0
	v_add_f32_e32 v0, v91, v0
	s_nop 1
	v_mov_b32_dpp v35, v0 quad_perm:[1,0,3,2] row_mask:0xf bank_mask:0xf
	v_cvt_pk_bf16_f32 v54, v54, v55
	v_cvt_pk_bf16_f32 v55, v62, v63
	v_cvt_pk_bf16_f32 v56, v64, v65
	v_cvt_pk_bf16_f32 v57, v88, v89
	s_waitcnt lgkmcnt(0)
	v_add_f32_e32 v0, v0, v35
	s_nop 1
	v_mov_b32_dpp v35, v0 quad_perm:[2,3,0,1] row_mask:0xf bank_mask:0xf
	s_waitcnt lgkmcnt(0)
	v_add_f32_e32 v0, v0, v35
	s_nop 1
	v_mov_b32_dpp v35, v0 row_half_mirror row_mask:0xf bank_mask:0xf
	s_waitcnt lgkmcnt(0)
	v_add_f32_e32 v35, v0, v35
	s_nop 1
	v_mov_b32_dpp v36, v35 row_mirror row_mask:0xf bank_mask:0xf
	v_xor_b32_e32 v0, s14, v187
	v_lshlrev_b32_e32 v0, 4, v0
	v_add3_u32 v0, 0, v0, v92
	ds_write_b128 v0, v[54:57] offset:256
	s_and_saveexec_b64 s[12:13], s[10:11]
	s_cbranch_execz .LBB0_334
	s_waitcnt lgkmcnt(1)
	v_add_f32_e32 v0, v35, v36
	v_add_u32_e32 v35, 0x20204, v94
	ds_write_b32 v35, v0

.LBB0_337:
	v_pk_mul_f32 v[36:37], v[14:15], v[68:69]
	v_lshlrev_b32_e32 v90, 16, v50
	v_pk_fma_f32 v[36:37], v[6:7], v[72:73], v[36:37]
	v_and_b32_e32 v91, 0xffff0000, v50
	v_pk_fma_f32 v[36:37], v[26:27], v[86:87], v[36:37]
	v_lshlrev_b32_e32 v88, 16, v51
	v_pk_fma_f32 v[36:37], v[38:39], v[90:91], v[36:37]
	v_and_b32_e32 v89, 0xffff0000, v51
	v_mul_f32_e32 v0, 0xbfb8aa3b, v36
	v_exp_f32_e32 v0, v0
	v_mul_f32_e32 v35, 0xbfb8aa3b, v37
	v_exp_f32_e32 v35, v35
	v_add_f32_e32 v0, 1.0, v0
	v_rcp_f32_e32 v54, v0
	v_add_f32_e32 v0, 1.0, v35
	v_rcp_f32_e32 v55, v0
	s_nop 0
	v_pk_mul_f32 v[54:55], v[36:37], v[54:55]
	v_pk_mul_f32 v[36:37], v[16:17], v[58:59]
	v_pk_mul_f32 v[56:57], v[54:55], v[54:55]
	v_pk_fma_f32 v[36:37], v[8:9], v[74:75], v[36:37]
	v_pk_mul_f32 v[74:75], v[18:19], v[70:71]
	v_pk_fma_f32 v[36:37], v[28:29], v[84:85], v[36:37]
	v_pk_fma_f32 v[74:75], v[10:11], v[76:77], v[74:75]
	v_pk_fma_f32 v[36:37], v[40:41], v[88:89], v[36:37]
	v_pk_fma_f32 v[76:77], v[30:31], v[82:83], v[74:75]
	v_mul_f32_e32 v0, 0xbfb8aa3b, v36
	v_exp_f32_e32 v0, v0
	v_mul_f32_e32 v35, 0xbfb8aa3b, v37
	v_exp_f32_e32 v35, v35
	v_lshlrev_b32_e32 v74, 16, v52
	v_add_f32_e32 v0, 1.0, v0
	v_rcp_f32_e32 v72, v0
	v_add_f32_e32 v0, 1.0, v35
	v_rcp_f32_e32 v73, v0
	v_and_b32_e32 v75, 0xffff0000, v52
	v_pk_fma_f32 v[76:77], v[42:43], v[74:75], v[76:77]
	v_cvt_pk_bf16_f32 v54, v54, v55
	v_mul_f32_e32 v0, 0xbfb8aa3b, v76
	v_exp_f32_e32 v0, v0
	v_mul_f32_e32 v35, 0xbfb8aa3b, v77
	v_exp_f32_e32 v35, v35
	v_pk_mul_f32 v[96:97], v[36:37], v[72:73]
	v_pk_mul_f32 v[72:73], v[20:21], v[60:61]
	v_add_f32_e32 v0, 1.0, v0
	v_pk_fma_f32 v[72:73], v[12:13], v[78:79], v[72:73]
	v_rcp_f32_e32 v36, v0
	v_pk_fma_f32 v[78:79], v[32:33], v[80:81], v[72:73]
	v_lshlrev_b32_e32 v72, 16, v53
	v_and_b32_e32 v73, 0xffff0000, v53
	v_pk_fma_f32 v[78:79], v[44:45], v[72:73], v[78:79]
	v_add_f32_e32 v0, 1.0, v35
	v_mul_f32_e32 v35, 0xbfb8aa3b, v78
	v_exp_f32_e32 v35, v35
	v_mul_f32_e32 v37, 0xbfb8aa3b, v79
	v_exp_f32_e32 v95, v37
	v_rcp_f32_e32 v37, v0
	v_add_f32_e32 v0, 1.0, v35
	v_rcp_f32_e32 v100, v0
	v_add_f32_e32 v0, 1.0, v95
	v_rcp_f32_e32 v101, v0
	v_pk_mul_f32 v[102:103], v[96:97], v[96:97]
	v_add_f32_e32 v0, v56, v57
	v_pk_mul_f32 v[76:77], v[76:77], v[36:37]
	v_add_f32_e32 v0, v102, v0
	v_pk_mul_f32 v[36:37], v[76:77], v[76:77]
	v_add_f32_e32 v0, v103, v0
	v_pk_mul_f32 v[78:79], v[78:79], v[100:101]
	v_add_f32_e32 v0, v36, v0
	v_pk_mul_f32 v[100:101], v[78:79], v[78:79]
	v_add_f32_e32 v0, v37, v0
	v_add_f32_e32 v0, v100, v0
	v_add_f32_e32 v0, v101, v0
	s_nop 1
	v_mov_b32_dpp v35, v0 quad_perm:[1,0,3,2] row_mask:0xf bank_mask:0xf
	v_cvt_pk_bf16_f32 v55, v96, v97
	v_cvt_pk_bf16_f32 v56, v76, v77
	v_cvt_pk_bf16_f32 v57, v78, v79
	s_waitcnt lgkmcnt(0)
	v_add_f32_e32 v0, v0, v35
	s_nop 1
	v_mov_b32_dpp v35, v0 quad_perm:[2,3,0,1] row_mask:0xf bank_mask:0xf
	s_waitcnt lgkmcnt(0)
	v_add_f32_e32 v0, v0, v35
	s_nop 1
	v_mov_b32_dpp v35, v0 row_half_mirror row_mask:0xf bank_mask:0xf
	s_waitcnt lgkmcnt(0)
	v_add_f32_e32 v35, v0, v35
	s_nop 1
	v_mov_b32_dpp v36, v35 row_mirror row_mask:0xf bank_mask:0xf
	v_xor_b32_e32 v0, s14, v187
	v_lshlrev_b32_e32 v0, 4, v0
	v_add3_u32 v0, 0, v0, v92
	ds_write_b128 v0, v[54:57] offset:512
	s_and_saveexec_b64 s[12:13], s[10:11]
	s_cbranch_execz .LBB0_339
	s_waitcnt lgkmcnt(1)
	v_add_f32_e32 v0, v35, v36
	v_add_u32_e32 v35, 0x20208, v94
	ds_write_b32 v35, v0

.LBB0_342:
	s_waitcnt lgkmcnt(1)
	v_pk_mul_f32 v[36:37], v[14:15], v[86:87]
	v_pk_mul_f32 v[78:79], v[18:19], v[82:83]
	v_pk_fma_f32 v[36:37], v[6:7], v[68:69], v[36:37]
	s_waitcnt vmcnt(0)
	v_lshlrev_b32_e32 v68, 16, v22
	v_pk_fma_f32 v[36:37], v[26:27], v[90:91], v[36:37]
	v_and_b32_e32 v69, 0xffff0000, v22
	v_pk_fma_f32 v[36:37], v[38:39], v[68:69], v[36:37]
	v_pk_fma_f32 v[70:71], v[10:11], v[70:71], v[78:79]
	v_mul_f32_e32 v0, 0xbfb8aa3b, v36
	v_exp_f32_e32 v0, v0
	v_mul_f32_e32 v35, 0xbfb8aa3b, v37
	v_exp_f32_e32 v35, v35
	v_pk_fma_f32 v[70:71], v[30:31], v[74:75], v[70:71]
	v_add_f32_e32 v0, 1.0, v0
	v_rcp_f32_e32 v68, v0
	v_add_f32_e32 v0, 1.0, v35
	v_rcp_f32_e32 v69, v0
	v_lshlrev_b32_e32 v74, 16, v24
	v_and_b32_e32 v75, 0xffff0000, v24
	v_pk_fma_f32 v[70:71], v[42:43], v[74:75], v[70:71]
	v_pk_mul_f32 v[68:69], v[36:37], v[68:69]
	v_pk_mul_f32 v[36:37], v[16:17], v[84:85]
	s_nop 0
	v_pk_fma_f32 v[36:37], v[8:9], v[58:59], v[36:37]
	v_lshlrev_b32_e32 v58, 16, v23
	v_pk_fma_f32 v[36:37], v[28:29], v[88:89], v[36:37]
	v_and_b32_e32 v59, 0xffff0000, v23
	v_pk_fma_f32 v[36:37], v[40:41], v[58:59], v[36:37]
	v_pk_mul_f32 v[58:59], v[68:69], v[68:69]
	v_mul_f32_e32 v0, 0xbfb8aa3b, v36
	v_exp_f32_e32 v0, v0
	v_mul_f32_e32 v35, 0xbfb8aa3b, v37
	v_exp_f32_e32 v35, v35
	v_add_f32_e32 v0, 1.0, v0
	v_rcp_f32_e32 v76, v0
	v_add_f32_e32 v0, 1.0, v35
	v_rcp_f32_e32 v77, v0
	v_mul_f32_e32 v0, 0xbfb8aa3b, v70
	v_exp_f32_e32 v0, v0
	v_mul_f32_e32 v35, 0xbfb8aa3b, v71
	v_exp_f32_e32 v35, v35
	v_pk_mul_f32 v[74:75], v[36:37], v[76:77]
	v_pk_mul_f32 v[76:77], v[20:21], v[80:81]
	v_add_f32_e32 v0, 1.0, v0
	v_pk_fma_f32 v[60:61], v[12:13], v[60:61], v[76:77]
	v_rcp_f32_e32 v36, v0
	v_pk_fma_f32 v[60:61], v[32:33], v[72:73], v[60:61]
	v_lshlrev_b32_e32 v72, 16, v25
	v_and_b32_e32 v73, 0xffff0000, v25
	v_pk_fma_f32 v[60:61], v[44:45], v[72:73], v[60:61]
	v_add_f32_e32 v0, 1.0, v35
	v_mul_f32_e32 v35, 0xbfb8aa3b, v60
	v_exp_f32_e32 v35, v35
	v_mul_f32_e32 v37, 0xbfb8aa3b, v61
	v_exp_f32_e32 v73, v37
	v_rcp_f32_e32 v37, v0
	v_add_f32_e32 v0, 1.0, v35
	v_rcp_f32_e32 v72, v0
	v_add_f32_e32 v0, 1.0, v73
	v_rcp_f32_e32 v73, v0
	v_pk_mul_f32 v[76:77], v[74:75], v[74:75]
	v_add_f32_e32 v0, v58, v59
	v_pk_mul_f32 v[70:71], v[70:71], v[36:37]
	v_add_f32_e32 v0, v76, v0
	v_pk_mul_f32 v[36:37], v[70:71], v[70:71]
	v_add_f32_e32 v0, v77, v0
	v_pk_mul_f32 v[72:73], v[60:61], v[72:73]
	v_add_f32_e32 v0, v36, v0
	v_pk_mul_f32 v[60:61], v[72:73], v[72:73]
	v_add_f32_e32 v0, v37, v0
	v_add_f32_e32 v0, v60, v0
	v_add_f32_e32 v0, v61, v0
	s_nop 1
	v_mov_b32_dpp v35, v0 quad_perm:[1,0,3,2] row_mask:0xf bank_mask:0xf
	v_cvt_pk_bf16_f32 v58, v68, v69
	v_cvt_pk_bf16_f32 v59, v74, v75
	v_cvt_pk_bf16_f32 v60, v70, v71
	v_cvt_pk_bf16_f32 v61, v72, v73
	s_waitcnt lgkmcnt(0)
	v_add_f32_e32 v0, v0, v35
	s_nop 1
	v_mov_b32_dpp v35, v0 quad_perm:[2,3,0,1] row_mask:0xf bank_mask:0xf
	s_waitcnt lgkmcnt(0)
	v_add_f32_e32 v0, v0, v35
	s_nop 1
	v_mov_b32_dpp v35, v0 row_half_mirror row_mask:0xf bank_mask:0xf
	s_waitcnt lgkmcnt(0)
	v_add_f32_e32 v35, v0, v35
	s_nop 1
	v_mov_b32_dpp v36, v35 row_mirror row_mask:0xf bank_mask:0xf
	v_xor_b32_e32 v0, s14, v187
	v_lshlrev_b32_e32 v0, 4, v0
	v_add3_u32 v0, 0, v0, v92
	ds_write_b128 v0, v[58:61] offset:768
	s_and_saveexec_b64 s[12:13], s[10:11]
	s_cbranch_execz .LBB0_326
	s_waitcnt lgkmcnt(1)
	v_add_f32_e32 v0, v35, v36
	v_add_u32_e32 v35, 0x2020c, v94
	ds_write_b32 v35, v0
	s_branch .LBB0_326

.LBB0_358:
	s_waitcnt vmcnt(11)
	v_mov_b64_e32 v[154:155], v[100:101]
	v_lshlrev_b32_e32 v122, 16, v114
	v_and_b32_e32 v123, 0xffff0000, v114
	v_mov_b64_e32 v[152:153], v[98:99]
	s_waitcnt lgkmcnt(1)
	v_lshlrev_b32_e32 v36, 16, v126
	v_and_b32_e32 v37, 0xffff0000, v126
	s_waitcnt vmcnt(5)
	v_pk_mul_f32 v[98:99], v[14:15], v[122:123]
	v_lshlrev_b32_e32 v148, 16, v152
	v_pk_fma_f32 v[36:37], v[6:7], v[36:37], v[98:99]
	v_add_co_u32_e32 v98, vcc, 0xfffe7000, v142
	v_and_b32_e32 v149, 0xffff0000, v152
	s_nop 0
	v_addc_co_u32_e32 v99, vcc, -1, v143, vcc
	global_load_dwordx4 v[98:101], v[98:99], off offset:-3584
	s_waitcnt vmcnt(4)
	v_pk_fma_f32 v[36:37], v[26:27], v[148:149], v[36:37]
	v_lshlrev_b32_e32 v144, 16, v110
	v_and_b32_e32 v145, 0xffff0000, v110
	s_waitcnt vmcnt(2)
	v_pk_fma_f32 v[36:37], v[102:103], v[144:145], v[36:37]
	v_lshlrev_b32_e32 v150, 16, v153
	v_mul_f32_e32 v0, 0xbfb8aa3b, v36
	v_exp_f32_e32 v0, v0
	v_mul_f32_e32 v35, 0xbfb8aa3b, v37
	v_exp_f32_e32 v35, v35
	v_and_b32_e32 v151, 0xffff0000, v153
	v_add_f32_e32 v0, 1.0, v0
	v_rcp_f32_e32 v124, v0
	v_add_f32_e32 v0, 1.0, v35
	v_rcp_f32_e32 v125, v0
	v_lshlrev_b32_e32 v126, 16, v111
	v_lshlrev_b32_e32 v156, 16, v116
	v_and_b32_e32 v157, 0xffff0000, v116
	v_pk_mul_f32 v[158:159], v[36:37], v[124:125]
	v_lshlrev_b32_e32 v124, 16, v115
	v_and_b32_e32 v125, 0xffff0000, v115
	v_lshlrev_b32_e32 v36, 16, v127
	v_and_b32_e32 v37, 0xffff0000, v127
	v_pk_mul_f32 v[114:115], v[16:17], v[124:125]
	v_and_b32_e32 v127, 0xffff0000, v111
	v_pk_fma_f32 v[36:37], v[8:9], v[36:37], v[114:115]
	v_lshlrev_b32_e32 v146, 16, v128
	v_pk_fma_f32 v[36:37], v[28:29], v[150:151], v[36:37]
	v_and_b32_e32 v147, 0xffff0000, v128
	v_pk_fma_f32 v[36:37], v[104:105], v[126:127], v[36:37]
	v_pk_mul_f32 v[152:153], v[22:23], v[156:157]
	v_mul_f32_e32 v0, 0xbfb8aa3b, v36
	v_exp_f32_e32 v0, v0
	v_mul_f32_e32 v35, 0xbfb8aa3b, v37
	v_exp_f32_e32 v35, v35
	v_pk_fma_f32 v[146:147], v[10:11], v[146:147], v[152:153]
	v_add_f32_e32 v0, 1.0, v0
	v_rcp_f32_e32 v114, v0
	v_add_f32_e32 v0, 1.0, v35
	v_lshlrev_b32_e32 v152, 16, v154
	v_and_b32_e32 v153, 0xffff0000, v154
	v_rcp_f32_e32 v115, v0
	v_pk_fma_f32 v[160:161], v[30:31], v[152:153], v[146:147]
	v_lshlrev_b32_e32 v146, 16, v112
	v_and_b32_e32 v147, 0xffff0000, v112
	s_waitcnt vmcnt(1)
	v_pk_fma_f32 v[160:161], v[106:107], v[146:147], v[160:161]
	v_lshlrev_b32_e32 v164, 16, v117
	v_mul_f32_e32 v0, 0xbfb8aa3b, v160
	v_exp_f32_e32 v0, v0
	v_mul_f32_e32 v35, 0xbfb8aa3b, v161
	v_and_b32_e32 v165, 0xffff0000, v117
	v_exp_f32_e32 v35, v35
	v_pk_mul_f32 v[162:163], v[36:37], v[114:115]
	v_lshlrev_b32_e32 v114, 16, v129
	v_and_b32_e32 v115, 0xffff0000, v129
	v_pk_mul_f32 v[116:117], v[24:25], v[164:165]
	v_lshlrev_b32_e32 v154, 16, v155
	v_pk_fma_f32 v[114:115], v[12:13], v[114:115], v[116:117]
	v_and_b32_e32 v155, 0xffff0000, v155
	v_pk_fma_f32 v[114:115], v[32:33], v[154:155], v[114:115]
	v_lshlrev_b32_e32 v128, 16, v113
	v_and_b32_e32 v129, 0xffff0000, v113
	v_add_f32_e32 v0, 1.0, v0
	v_pk_fma_f32 v[112:113], v[108:109], v[128:129], v[114:115]
	v_rcp_f32_e32 v36, v0
	v_add_f32_e32 v0, 1.0, v35
	v_mul_f32_e32 v35, 0xbfb8aa3b, v112
	v_exp_f32_e32 v35, v35
	v_mul_f32_e32 v37, 0xbfb8aa3b, v113
	v_exp_f32_e32 v115, v37
	v_rcp_f32_e32 v37, v0
	v_add_f32_e32 v0, 1.0, v35
	v_rcp_f32_e32 v114, v0
	v_add_f32_e32 v0, 1.0, v115
	v_pk_mul_f32 v[110:111], v[158:159], v[158:159]
	v_rcp_f32_e32 v115, v0
	v_pk_mul_f32 v[116:117], v[162:163], v[162:163]
	v_add_f32_e32 v0, v110, v111
	v_pk_mul_f32 v[160:161], v[160:161], v[36:37]
	v_add_f32_e32 v0, v116, v0
	v_pk_mul_f32 v[36:37], v[160:161], v[160:161]
	v_add_f32_e32 v0, v117, v0
	v_pk_mul_f32 v[166:167], v[112:113], v[114:115]
	v_add_f32_e32 v0, v36, v0
	v_pk_mul_f32 v[112:113], v[166:167], v[166:167]
	v_add_f32_e32 v0, v37, v0
	v_add_f32_e32 v0, v112, v0
	v_add_f32_e32 v0, v113, v0
	s_nop 1
	v_mov_b32_dpp v35, v0 quad_perm:[1,0,3,2] row_mask:0xf bank_mask:0xf
	v_mov_b64_e32 v[114:115], v[118:119]
	v_mov_b64_e32 v[116:117], v[120:121]
	v_cvt_pk_bf16_f32 v110, v158, v159
	v_cvt_pk_bf16_f32 v111, v162, v163
	s_waitcnt lgkmcnt(0)
	v_add_f32_e32 v0, v0, v35
	s_nop 1
	v_mov_b32_dpp v35, v0 quad_perm:[2,3,0,1] row_mask:0xf bank_mask:0xf
	v_cvt_pk_bf16_f32 v112, v160, v161
	v_cvt_pk_bf16_f32 v113, v166, v167
	v_add_u32_e32 v218, 0, v217
	s_waitcnt lgkmcnt(0)
	v_add_f32_e32 v0, v0, v35
	s_nop 1
	v_mov_b32_dpp v35, v0 row_half_mirror row_mask:0xf bank_mask:0xf
	s_waitcnt lgkmcnt(0)
	v_add_f32_e32 v35, v0, v35
	s_nop 1
	v_mov_b32_dpp v36, v35 row_mirror row_mask:0xf bank_mask:0xf
	v_xor_b32_e32 v0, s14, v187
	v_lshlrev_b32_e32 v0, 4, v0
	v_add3_u32 v0, 0, v0, v216
	ds_write_b128 v0, v[110:113]
	s_and_saveexec_b64 s[12:13], s[10:11]
	s_cbranch_execz .LBB0_360
	s_waitcnt lgkmcnt(1)
	v_add_f32_e32 v0, v35, v36
	v_add_u32_e32 v35, 0x20200, v218
	ds_write_b32 v35, v0

.LBB0_363:
	v_pk_mul_f32 v[36:37], v[14:15], v[148:149]
	v_lshlrev_b32_e32 v162, 16, v2
	v_pk_fma_f32 v[36:37], v[6:7], v[122:123], v[36:37]
	v_and_b32_e32 v163, 0xffff0000, v2
	v_pk_fma_f32 v[36:37], v[26:27], v[144:145], v[36:37]
	v_lshlrev_b32_e32 v160, 16, v3
	v_pk_fma_f32 v[36:37], v[102:103], v[162:163], v[36:37]
	v_and_b32_e32 v161, 0xffff0000, v3
	v_mul_f32_e32 v0, 0xbfb8aa3b, v36
	v_exp_f32_e32 v0, v0
	v_mul_f32_e32 v35, 0xbfb8aa3b, v37
	v_exp_f32_e32 v35, v35
	v_lshlrev_b32_e32 v158, 16, v4
	v_add_f32_e32 v0, 1.0, v0
	v_rcp_f32_e32 v118, v0
	v_add_f32_e32 v0, 1.0, v35
	v_rcp_f32_e32 v119, v0
	v_and_b32_e32 v159, 0xffff0000, v4
	v_pk_mul_f32 v[118:119], v[36:37], v[118:119]
	v_pk_mul_f32 v[36:37], v[16:17], v[150:151]
	v_pk_mul_f32 v[120:121], v[118:119], v[118:119]
	v_pk_fma_f32 v[36:37], v[8:9], v[124:125], v[36:37]
	v_pk_mul_f32 v[124:125], v[22:23], v[152:153]
	v_pk_fma_f32 v[36:37], v[28:29], v[126:127], v[36:37]
	v_pk_fma_f32 v[124:125], v[10:11], v[156:157], v[124:125]
	v_pk_fma_f32 v[36:37], v[104:105], v[160:161], v[36:37]
	v_pk_fma_f32 v[124:125], v[30:31], v[146:147], v[124:125]
	v_mul_f32_e32 v0, 0xbfb8aa3b, v36
	v_exp_f32_e32 v0, v0
	v_mul_f32_e32 v35, 0xbfb8aa3b, v37
	v_exp_f32_e32 v35, v35
	v_pk_fma_f32 v[124:125], v[106:107], v[158:159], v[124:125]
	v_add_f32_e32 v0, 1.0, v0
	v_rcp_f32_e32 v122, v0
	v_add_f32_e32 v0, 1.0, v35
	v_rcp_f32_e32 v123, v0
	v_mul_f32_e32 v0, 0xbfb8aa3b, v124
	v_exp_f32_e32 v0, v0
	v_mul_f32_e32 v35, 0xbfb8aa3b, v125
	v_exp_f32_e32 v35, v35
	v_pk_mul_f32 v[156:157], v[24:25], v[154:155]
	v_add_f32_e32 v0, 1.0, v0
	v_pk_fma_f32 v[156:157], v[12:13], v[164:165], v[156:157]
	v_pk_mul_f32 v[122:123], v[36:37], v[122:123]
	v_pk_fma_f32 v[164:165], v[32:33], v[128:129], v[156:157]
	v_lshlrev_b32_e32 v156, 16, v5
	v_and_b32_e32 v157, 0xffff0000, v5
	v_pk_fma_f32 v[164:165], v[108:109], v[156:157], v[164:165]
	v_rcp_f32_e32 v36, v0
	v_add_f32_e32 v0, 1.0, v35
	v_mul_f32_e32 v35, 0xbfb8aa3b, v164
	v_exp_f32_e32 v35, v35
	v_mul_f32_e32 v37, 0xbfb8aa3b, v165
	v_exp_f32_e32 v167, v37
	v_rcp_f32_e32 v37, v0
	v_add_f32_e32 v0, 1.0, v35
	v_rcp_f32_e32 v166, v0
	v_add_f32_e32 v0, 1.0, v167
	v_rcp_f32_e32 v167, v0
	v_pk_mul_f32 v[220:221], v[122:123], v[122:123]
	v_add_f32_e32 v0, v120, v121
	v_pk_mul_f32 v[124:125], v[124:125], v[36:37]
	v_add_f32_e32 v0, v220, v0
	v_pk_mul_f32 v[36:37], v[124:125], v[124:125]
	v_add_f32_e32 v0, v221, v0
	v_pk_mul_f32 v[164:165], v[164:165], v[166:167]
	v_add_f32_e32 v0, v36, v0
	v_pk_mul_f32 v[166:167], v[164:165], v[164:165]
	v_add_f32_e32 v0, v37, v0
	v_add_f32_e32 v0, v166, v0
	v_add_f32_e32 v0, v167, v0
	s_nop 1
	v_mov_b32_dpp v35, v0 quad_perm:[1,0,3,2] row_mask:0xf bank_mask:0xf
	v_cvt_pk_bf16_f32 v118, v118, v119
	v_cvt_pk_bf16_f32 v119, v122, v123
	v_cvt_pk_bf16_f32 v120, v124, v125
	v_cvt_pk_bf16_f32 v121, v164, v165
	s_waitcnt lgkmcnt(0)
	v_add_f32_e32 v0, v0, v35
	s_nop 1
	v_mov_b32_dpp v35, v0 quad_perm:[2,3,0,1] row_mask:0xf bank_mask:0xf
	s_waitcnt lgkmcnt(0)
	v_add_f32_e32 v0, v0, v35
	s_nop 1
	v_mov_b32_dpp v35, v0 row_half_mirror row_mask:0xf bank_mask:0xf
	s_waitcnt lgkmcnt(0)
	v_add_f32_e32 v35, v0, v35
	s_nop 1
	v_mov_b32_dpp v36, v35 row_mirror row_mask:0xf bank_mask:0xf
	v_xor_b32_e32 v0, s14, v187
	v_lshlrev_b32_e32 v0, 4, v0
	v_add3_u32 v0, 0, v0, v216
	ds_write_b128 v0, v[118:121] offset:256
	s_and_saveexec_b64 s[12:13], s[10:11]
	s_cbranch_execz .LBB0_365
	s_waitcnt lgkmcnt(1)
	v_add_f32_e32 v0, v35, v36
	v_add_u32_e32 v35, 0x20204, v218
	ds_write_b32 v35, v0

.LBB0_368:
	v_pk_mul_f32 v[36:37], v[14:15], v[144:145]
	v_lshlrev_b32_e32 v166, 16, v114
	v_pk_fma_f32 v[36:37], v[6:7], v[148:149], v[36:37]
	v_and_b32_e32 v167, 0xffff0000, v114
	v_pk_fma_f32 v[36:37], v[26:27], v[162:163], v[36:37]
	v_lshlrev_b32_e32 v164, 16, v115
	v_pk_fma_f32 v[36:37], v[102:103], v[166:167], v[36:37]
	v_and_b32_e32 v165, 0xffff0000, v115
	v_mul_f32_e32 v0, 0xbfb8aa3b, v36
	v_exp_f32_e32 v0, v0
	v_mul_f32_e32 v35, 0xbfb8aa3b, v37
	v_exp_f32_e32 v35, v35
	v_add_f32_e32 v0, 1.0, v0
	v_rcp_f32_e32 v118, v0
	v_add_f32_e32 v0, 1.0, v35
	v_rcp_f32_e32 v119, v0
	s_nop 0
	v_pk_mul_f32 v[118:119], v[36:37], v[118:119]
	v_pk_mul_f32 v[36:37], v[16:17], v[126:127]
	v_pk_mul_f32 v[120:121], v[118:119], v[118:119]
	v_pk_fma_f32 v[36:37], v[8:9], v[150:151], v[36:37]
	v_pk_mul_f32 v[150:151], v[22:23], v[146:147]
	v_pk_fma_f32 v[36:37], v[28:29], v[160:161], v[36:37]
	v_pk_fma_f32 v[150:151], v[10:11], v[152:153], v[150:151]
	v_pk_fma_f32 v[36:37], v[104:105], v[164:165], v[36:37]
	v_pk_fma_f32 v[152:153], v[30:31], v[158:159], v[150:151]
	v_mul_f32_e32 v0, 0xbfb8aa3b, v36
	v_exp_f32_e32 v0, v0
	v_mul_f32_e32 v35, 0xbfb8aa3b, v37
	v_exp_f32_e32 v35, v35
	v_lshlrev_b32_e32 v150, 16, v116
	v_add_f32_e32 v0, 1.0, v0
	v_rcp_f32_e32 v148, v0
	v_add_f32_e32 v0, 1.0, v35
	v_rcp_f32_e32 v149, v0
	v_and_b32_e32 v151, 0xffff0000, v116
	v_pk_fma_f32 v[152:153], v[106:107], v[150:151], v[152:153]
	v_cvt_pk_bf16_f32 v118, v118, v119
	v_mul_f32_e32 v0, 0xbfb8aa3b, v152
	v_exp_f32_e32 v0, v0
	v_mul_f32_e32 v35, 0xbfb8aa3b, v153
	v_exp_f32_e32 v35, v35
	v_pk_mul_f32 v[220:221], v[36:37], v[148:149]
	v_pk_mul_f32 v[148:149], v[24:25], v[128:129]
	v_add_f32_e32 v0, 1.0, v0
	v_pk_fma_f32 v[148:149], v[12:13], v[154:155], v[148:149]
	v_rcp_f32_e32 v36, v0
	v_pk_fma_f32 v[154:155], v[32:33], v[156:157], v[148:149]
	v_lshlrev_b32_e32 v148, 16, v117
	v_and_b32_e32 v149, 0xffff0000, v117
	v_pk_fma_f32 v[154:155], v[108:109], v[148:149], v[154:155]
	v_add_f32_e32 v0, 1.0, v35
	v_mul_f32_e32 v35, 0xbfb8aa3b, v154
	v_exp_f32_e32 v35, v35
	v_mul_f32_e32 v37, 0xbfb8aa3b, v155
	v_exp_f32_e32 v219, v37
	v_rcp_f32_e32 v37, v0
	v_add_f32_e32 v0, 1.0, v35
	v_rcp_f32_e32 v222, v0
	v_add_f32_e32 v0, 1.0, v219
	v_rcp_f32_e32 v223, v0
	v_pk_mul_f32 v[224:225], v[220:221], v[220:221]
	v_add_f32_e32 v0, v120, v121
	v_pk_mul_f32 v[152:153], v[152:153], v[36:37]
	v_add_f32_e32 v0, v224, v0
	v_pk_mul_f32 v[36:37], v[152:153], v[152:153]
	v_add_f32_e32 v0, v225, v0
	v_pk_mul_f32 v[154:155], v[154:155], v[222:223]
	v_add_f32_e32 v0, v36, v0
	v_pk_mul_f32 v[222:223], v[154:155], v[154:155]
	v_add_f32_e32 v0, v37, v0
	v_add_f32_e32 v0, v222, v0
	v_add_f32_e32 v0, v223, v0
	s_nop 1
	v_mov_b32_dpp v35, v0 quad_perm:[1,0,3,2] row_mask:0xf bank_mask:0xf
	v_cvt_pk_bf16_f32 v119, v220, v221
	v_cvt_pk_bf16_f32 v120, v152, v153
	v_cvt_pk_bf16_f32 v121, v154, v155
	s_waitcnt lgkmcnt(0)
	v_add_f32_e32 v0, v0, v35
	s_nop 1
	v_mov_b32_dpp v35, v0 quad_perm:[2,3,0,1] row_mask:0xf bank_mask:0xf
	s_waitcnt lgkmcnt(0)
	v_add_f32_e32 v0, v0, v35
	s_nop 1
	v_mov_b32_dpp v35, v0 row_half_mirror row_mask:0xf bank_mask:0xf
	s_waitcnt lgkmcnt(0)
	v_add_f32_e32 v35, v0, v35
	s_nop 1
	v_mov_b32_dpp v36, v35 row_mirror row_mask:0xf bank_mask:0xf
	v_xor_b32_e32 v0, s14, v187
	v_lshlrev_b32_e32 v0, 4, v0
	v_add3_u32 v0, 0, v0, v216
	ds_write_b128 v0, v[118:121] offset:512
	s_and_saveexec_b64 s[12:13], s[10:11]
	s_cbranch_execz .LBB0_370
	s_waitcnt lgkmcnt(1)
	v_add_f32_e32 v0, v35, v36
	v_add_u32_e32 v35, 0x20208, v218
	ds_write_b32 v35, v0

.LBB0_373:
	s_waitcnt lgkmcnt(1)
	v_pk_mul_f32 v[36:37], v[14:15], v[162:163]
	v_pk_mul_f32 v[154:155], v[22:23], v[158:159]
	v_pk_fma_f32 v[36:37], v[6:7], v[144:145], v[36:37]
	s_waitcnt vmcnt(0)
	v_lshlrev_b32_e32 v144, 16, v98
	v_pk_fma_f32 v[36:37], v[26:27], v[166:167], v[36:37]
	v_and_b32_e32 v145, 0xffff0000, v98
	v_pk_fma_f32 v[36:37], v[102:103], v[144:145], v[36:37]
	v_pk_fma_f32 v[146:147], v[10:11], v[146:147], v[154:155]
	v_mul_f32_e32 v0, 0xbfb8aa3b, v36
	v_exp_f32_e32 v0, v0
	v_mul_f32_e32 v35, 0xbfb8aa3b, v37
	v_exp_f32_e32 v35, v35
	v_pk_fma_f32 v[146:147], v[30:31], v[150:151], v[146:147]
	v_add_f32_e32 v0, 1.0, v0
	v_rcp_f32_e32 v144, v0
	v_add_f32_e32 v0, 1.0, v35
	v_rcp_f32_e32 v145, v0
	v_lshlrev_b32_e32 v150, 16, v100
	v_and_b32_e32 v151, 0xffff0000, v100
	v_pk_fma_f32 v[146:147], v[106:107], v[150:151], v[146:147]
	v_pk_mul_f32 v[144:145], v[36:37], v[144:145]
	v_pk_mul_f32 v[36:37], v[16:17], v[160:161]
	s_nop 0
	v_pk_fma_f32 v[36:37], v[8:9], v[126:127], v[36:37]
	v_lshlrev_b32_e32 v126, 16, v99
	v_pk_fma_f32 v[36:37], v[28:29], v[164:165], v[36:37]
	v_and_b32_e32 v127, 0xffff0000, v99
	v_pk_fma_f32 v[36:37], v[104:105], v[126:127], v[36:37]
	v_pk_mul_f32 v[126:127], v[144:145], v[144:145]
	v_mul_f32_e32 v0, 0xbfb8aa3b, v36
	v_exp_f32_e32 v0, v0
	v_mul_f32_e32 v35, 0xbfb8aa3b, v37
	v_exp_f32_e32 v35, v35
	v_add_f32_e32 v0, 1.0, v0
	v_rcp_f32_e32 v152, v0
	v_add_f32_e32 v0, 1.0, v35
	v_rcp_f32_e32 v153, v0
	v_mul_f32_e32 v0, 0xbfb8aa3b, v146
	v_exp_f32_e32 v0, v0
	v_mul_f32_e32 v35, 0xbfb8aa3b, v147
	v_exp_f32_e32 v35, v35
	v_pk_mul_f32 v[150:151], v[36:37], v[152:153]
	v_pk_mul_f32 v[152:153], v[24:25], v[156:157]
	v_add_f32_e32 v0, 1.0, v0
	v_pk_fma_f32 v[128:129], v[12:13], v[128:129], v[152:153]
	v_rcp_f32_e32 v36, v0
	v_pk_fma_f32 v[128:129], v[32:33], v[148:149], v[128:129]
	v_lshlrev_b32_e32 v148, 16, v101
	v_and_b32_e32 v149, 0xffff0000, v101
	v_pk_fma_f32 v[128:129], v[108:109], v[148:149], v[128:129]
	v_add_f32_e32 v0, 1.0, v35
	v_mul_f32_e32 v35, 0xbfb8aa3b, v128
	v_exp_f32_e32 v35, v35
	v_mul_f32_e32 v37, 0xbfb8aa3b, v129
	v_exp_f32_e32 v149, v37
	v_rcp_f32_e32 v37, v0
	v_add_f32_e32 v0, 1.0, v35
	v_rcp_f32_e32 v148, v0
	v_add_f32_e32 v0, 1.0, v149
	v_rcp_f32_e32 v149, v0
	v_pk_mul_f32 v[152:153], v[150:151], v[150:151]
	v_add_f32_e32 v0, v126, v127
	v_pk_mul_f32 v[146:147], v[146:147], v[36:37]
	v_add_f32_e32 v0, v152, v0
	v_pk_mul_f32 v[36:37], v[146:147], v[146:147]
	v_add_f32_e32 v0, v153, v0
	v_pk_mul_f32 v[148:149], v[128:129], v[148:149]
	v_add_f32_e32 v0, v36, v0
	v_pk_mul_f32 v[128:129], v[148:149], v[148:149]
	v_add_f32_e32 v0, v37, v0
	v_add_f32_e32 v0, v128, v0
	v_add_f32_e32 v0, v129, v0
	s_nop 1
	v_mov_b32_dpp v35, v0 quad_perm:[1,0,3,2] row_mask:0xf bank_mask:0xf
	v_cvt_pk_bf16_f32 v126, v144, v145
	v_cvt_pk_bf16_f32 v127, v150, v151
	v_cvt_pk_bf16_f32 v128, v146, v147
	v_cvt_pk_bf16_f32 v129, v148, v149
	s_waitcnt lgkmcnt(0)
	v_add_f32_e32 v0, v0, v35
	s_nop 1
	v_mov_b32_dpp v35, v0 quad_perm:[2,3,0,1] row_mask:0xf bank_mask:0xf
	s_waitcnt lgkmcnt(0)
	v_add_f32_e32 v0, v0, v35
	s_nop 1
	v_mov_b32_dpp v35, v0 row_half_mirror row_mask:0xf bank_mask:0xf
	s_waitcnt lgkmcnt(0)
	v_add_f32_e32 v35, v0, v35
	s_nop 1
	v_mov_b32_dpp v36, v35 row_mirror row_mask:0xf bank_mask:0xf
	v_xor_b32_e32 v0, s14, v187
	v_lshlrev_b32_e32 v0, 4, v0
	v_add3_u32 v0, 0, v0, v216
	ds_write_b128 v0, v[126:129] offset:768
	s_and_saveexec_b64 s[12:13], s[10:11]
	s_cbranch_execz .LBB0_357
	s_waitcnt lgkmcnt(1)
	v_add_f32_e32 v0, v35, v36
	v_add_u32_e32 v35, 0x2020c, v218
	ds_write_b32 v35, v0
	s_branch .LBB0_357
